# final RMSNorm: as previous plus lane owns 4 consecutive floats per 256-col block so every output store instruction writes 1 KB contiguous (was alternating 16B chunks)
# speedup vs baseline: 1.0128x; 1.0028x over previous
.LBB0_3638:
	s_or_b64 exec, exec, s[6:7]
	s_lshr_b32 s1, s97, 3
	s_mul_i32 s1, s1, s64
	v_readlane_b32 s3, v254, 12
	s_and_b32 s0, s97, 7
	s_add_i32 s1, s1, s3
	s_cmp_eq_u32 s0, 0
	s_cselect_b32 s0, s1, s2
	s_waitcnt lgkmcnt(0)
	s_barrier
	s_lshl_b32 s1, s0, 3
	s_nop 0
	v_readfirstlane_b32 s0, v0
	s_lshl_b32 s13, s97, 3
	s_ashr_i32 s2, s0, 6
	s_add_i32 s12, s2, s1
	s_cmp_lt_i32 s12, 0x10000
	s_cbranch_scc0 .LBB0_3641
	s_load_dwordx4 s[4:7], s[90:91], 0xc0
	s_load_dwordx2 s[8:9], s[90:91], 0x28
	v_and_b32_e32 v1, 63, v0
	v_lshlrev_b32_e32 v2, 4, v1
	v_lshlrev_b32_e32 v3, 3, v1
	v_and_b32_e32 v4, 15, v1
	v_lshlrev_b32_e32 v4, 18, v4
	v_mov_b32_e32 v5, 0x358637bd
	s_lshl_b32 s20, s13, 2
	s_lshl_b32 s21, s13, 11
	s_lshl_b32 s22, s13, 12
	s_mul_i32 s23, s13, 7
	s_waitcnt lgkmcnt(0)
	global_load_dwordx4 v[8:11], v2, s[8:9] offset:0
	global_load_dwordx4 v[12:15], v2, s[8:9] offset:1024
	global_load_dwordx4 v[16:19], v2, s[8:9] offset:2048
	global_load_dwordx4 v[20:23], v2, s[8:9] offset:3072
	s_ashr_i32 s15, s12, 31
	s_mov_b32 s14, s12
	s_lshl_b64 s[16:17], s[14:15], 2
	s_add_u32 s16, s16, 0x72000000
	s_addc_u32 s17, s17, 0
	s_add_u32 s16, s16, s6
	s_addc_u32 s17, s17, s7
	s_lshl_b64 s[18:19], s[14:15], 11
	s_add_u32 s18, s18, 0x26c00000
	s_addc_u32 s19, s19, 0
	s_add_u32 s18, s18, s6
	s_addc_u32 s19, s19, s7
	s_lshl_b64 s[24:25], s[14:15], 12
	s_add_u32 s24, s24, s4
	s_addc_u32 s25, s25, s5
	s_add_i32 s14, s12, s23
	s_cmp_lt_i32 s14, 0x10000
	s_cbranch_scc0 .Lfin_tail
	s_mov_b64 s[26:27], s[16:17]
	s_mov_b64 s[28:29], s[18:19]
	global_load_dword v40, v4, s[26:27]
	global_load_dwordx2 v[32:33], v3, s[28:29] offset:0
	global_load_dwordx2 v[34:35], v3, s[28:29] offset:512
	global_load_dwordx2 v[36:37], v3, s[28:29] offset:1024
	global_load_dwordx2 v[38:39], v3, s[28:29] offset:1536
	s_add_u32 s16, s16, s20
	s_addc_u32 s17, s17, 0
	s_add_u32 s18, s18, s21
	s_addc_u32 s19, s19, 0
	s_add_i32 s12, s12, s13
	s_mov_b64 s[30:31], s[16:17]
	s_mov_b64 s[32:33], s[18:19]
	global_load_dword v50, v4, s[30:31]
	global_load_dwordx2 v[42:43], v3, s[32:33] offset:0
	global_load_dwordx2 v[44:45], v3, s[32:33] offset:512
	global_load_dwordx2 v[46:47], v3, s[32:33] offset:1024
	global_load_dwordx2 v[48:49], v3, s[32:33] offset:1536
	s_add_u32 s16, s16, s20
	s_addc_u32 s17, s17, 0
	s_add_u32 s18, s18, s21
	s_addc_u32 s19, s19, 0
	s_add_i32 s12, s12, s13
	s_mov_b64 s[26:27], s[16:17]
	s_mov_b64 s[28:29], s[18:19]
	global_load_dword v60, v4, s[26:27]
	global_load_dwordx2 v[52:53], v3, s[28:29] offset:0
	global_load_dwordx2 v[54:55], v3, s[28:29] offset:512
	global_load_dwordx2 v[56:57], v3, s[28:29] offset:1024
	global_load_dwordx2 v[58:59], v3, s[28:29] offset:1536
	s_add_u32 s16, s16, s20
	s_addc_u32 s17, s17, 0
	s_add_u32 s18, s18, s21
	s_addc_u32 s19, s19, 0
	s_add_i32 s12, s12, s13
	s_mov_b64 s[30:31], s[16:17]
	s_mov_b64 s[32:33], s[18:19]
	global_load_dword v70, v4, s[30:31]
	global_load_dwordx2 v[62:63], v3, s[32:33] offset:0
	global_load_dwordx2 v[64:65], v3, s[32:33] offset:512
	global_load_dwordx2 v[66:67], v3, s[32:33] offset:1024
	global_load_dwordx2 v[68:69], v3, s[32:33] offset:1536
	s_add_u32 s16, s16, s20
	s_addc_u32 s17, s17, 0
	s_add_u32 s18, s18, s21
	s_addc_u32 s19, s19, 0
	s_add_i32 s12, s12, s13
	s_mov_b64 s[26:27], s[16:17]
	s_mov_b64 s[28:29], s[18:19]
	global_load_dword v80, v4, s[26:27]
	global_load_dwordx2 v[72:73], v3, s[28:29] offset:0
	global_load_dwordx2 v[74:75], v3, s[28:29] offset:512
	global_load_dwordx2 v[76:77], v3, s[28:29] offset:1024
	global_load_dwordx2 v[78:79], v3, s[28:29] offset:1536
	s_add_u32 s16, s16, s20
	s_addc_u32 s17, s17, 0
	s_add_u32 s18, s18, s21
	s_addc_u32 s19, s19, 0
	s_add_i32 s12, s12, s13
	s_mov_b64 s[30:31], s[16:17]
	s_mov_b64 s[32:33], s[18:19]
	global_load_dword v90, v4, s[30:31]
	global_load_dwordx2 v[82:83], v3, s[32:33] offset:0
	global_load_dwordx2 v[84:85], v3, s[32:33] offset:512
	global_load_dwordx2 v[86:87], v3, s[32:33] offset:1024
	global_load_dwordx2 v[88:89], v3, s[32:33] offset:1536
	s_add_u32 s16, s16, s20
	s_addc_u32 s17, s17, 0
	s_add_u32 s18, s18, s21
	s_addc_u32 s19, s19, 0
	s_add_i32 s12, s12, s13
	s_mov_b64 s[26:27], s[16:17]
	s_mov_b64 s[28:29], s[18:19]
	global_load_dword v100, v4, s[26:27]
	global_load_dwordx2 v[92:93], v3, s[28:29] offset:0
	global_load_dwordx2 v[94:95], v3, s[28:29] offset:512
	global_load_dwordx2 v[96:97], v3, s[28:29] offset:1024
	global_load_dwordx2 v[98:99], v3, s[28:29] offset:1536
	s_add_u32 s16, s16, s20
	s_addc_u32 s17, s17, 0
	s_add_u32 s18, s18, s21
	s_addc_u32 s19, s19, 0
	s_add_i32 s12, s12, s13
	s_mov_b64 s[30:31], s[16:17]
	s_mov_b64 s[32:33], s[18:19]
	global_load_dword v110, v4, s[30:31]
	global_load_dwordx2 v[102:103], v3, s[32:33] offset:0
	global_load_dwordx2 v[104:105], v3, s[32:33] offset:512
	global_load_dwordx2 v[106:107], v3, s[32:33] offset:1024
	global_load_dwordx2 v[108:109], v3, s[32:33] offset:1536
	s_add_u32 s16, s16, s20
	s_addc_u32 s17, s17, 0
	s_add_u32 s18, s18, s21
	s_addc_u32 s19, s19, 0
	s_add_i32 s12, s12, s13
	s_waitcnt vmcnt(35)
	v_add_f32_dpp v112, v40, v40 quad_perm:[1,0,3,2] row_mask:0xf bank_mask:0xf
	s_mov_b64 s[34:35], s[24:25]
	s_add_u32 s24, s24, s22
	v_add_f32_dpp v112, v112, v112 quad_perm:[2,3,0,1] row_mask:0xf bank_mask:0xf
	s_addc_u32 s25, s25, 0
	s_nop 0
	v_add_f32_dpp v112, v112, v112 row_half_mirror row_mask:0xf bank_mask:0xf
	s_nop 1
	v_add_f32_dpp v112, v112, v112 row_mirror row_mask:0xf bank_mask:0xf
	v_fmamk_f32 v112, v112, 0x3a800000, v5
	v_rsq_f32_e32 v114, v112
	v_lshlrev_b32_e32 v116, 16, v32
	v_and_b32_e32 v117, 0xffff0000, v32
	v_lshlrev_b32_e32 v118, 16, v33
	v_and_b32_e32 v119, 0xffff0000, v33
	v_lshlrev_b32_e32 v120, 16, v34
	v_and_b32_e32 v121, 0xffff0000, v34
	v_lshlrev_b32_e32 v122, 16, v35
	v_and_b32_e32 v123, 0xffff0000, v35
	v_lshlrev_b32_e32 v124, 16, v36
	v_and_b32_e32 v125, 0xffff0000, v36
	v_lshlrev_b32_e32 v126, 16, v37
	v_and_b32_e32 v127, 0xffff0000, v37
	v_lshlrev_b32_e32 v128, 16, v38
	v_and_b32_e32 v129, 0xffff0000, v38
	v_lshlrev_b32_e32 v130, 16, v39
	v_and_b32_e32 v131, 0xffff0000, v39
	v_pk_mul_f32 v[116:117], v[114:115], v[116:117] op_sel_hi:[0,1]
	v_pk_mul_f32 v[118:119], v[114:115], v[118:119] op_sel_hi:[0,1]
	v_pk_mul_f32 v[120:121], v[114:115], v[120:121] op_sel_hi:[0,1]
	v_pk_mul_f32 v[122:123], v[114:115], v[122:123] op_sel_hi:[0,1]
	v_pk_mul_f32 v[124:125], v[114:115], v[124:125] op_sel_hi:[0,1]
	v_pk_mul_f32 v[126:127], v[114:115], v[126:127] op_sel_hi:[0,1]
	v_pk_mul_f32 v[128:129], v[114:115], v[128:129] op_sel_hi:[0,1]
	v_pk_mul_f32 v[130:131], v[114:115], v[130:131] op_sel_hi:[0,1]
	v_pk_mul_f32 v[132:133], v[8:9], v[116:117]
	v_pk_mul_f32 v[134:135], v[10:11], v[118:119]
	v_pk_mul_f32 v[136:137], v[12:13], v[120:121]
	v_pk_mul_f32 v[138:139], v[14:15], v[122:123]
	v_pk_mul_f32 v[140:141], v[16:17], v[124:125]
	v_pk_mul_f32 v[142:143], v[18:19], v[126:127]
	v_pk_mul_f32 v[144:145], v[20:21], v[128:129]
	v_pk_mul_f32 v[146:147], v[22:23], v[130:131]
	global_store_dwordx4 v2, v[132:135], s[34:35] offset:0
	global_store_dwordx4 v2, v[136:139], s[34:35] offset:1024
	global_store_dwordx4 v2, v[140:143], s[34:35] offset:2048
	global_store_dwordx4 v2, v[144:147], s[34:35] offset:3072
	s_waitcnt vmcnt(34)
	v_add_f32_dpp v112, v50, v50 quad_perm:[1,0,3,2] row_mask:0xf bank_mask:0xf
	s_mov_b64 s[36:37], s[24:25]
	s_add_u32 s24, s24, s22
	v_add_f32_dpp v112, v112, v112 quad_perm:[2,3,0,1] row_mask:0xf bank_mask:0xf
	s_addc_u32 s25, s25, 0
	s_nop 0
	v_add_f32_dpp v112, v112, v112 row_half_mirror row_mask:0xf bank_mask:0xf
	s_nop 1
	v_add_f32_dpp v112, v112, v112 row_mirror row_mask:0xf bank_mask:0xf
	v_fmamk_f32 v112, v112, 0x3a800000, v5
	v_rsq_f32_e32 v114, v112
	v_lshlrev_b32_e32 v116, 16, v42
	v_and_b32_e32 v117, 0xffff0000, v42
	v_lshlrev_b32_e32 v118, 16, v43
	v_and_b32_e32 v119, 0xffff0000, v43
	v_lshlrev_b32_e32 v120, 16, v44
	v_and_b32_e32 v121, 0xffff0000, v44
	v_lshlrev_b32_e32 v122, 16, v45
	v_and_b32_e32 v123, 0xffff0000, v45
	v_lshlrev_b32_e32 v124, 16, v46
	v_and_b32_e32 v125, 0xffff0000, v46
	v_lshlrev_b32_e32 v126, 16, v47
	v_and_b32_e32 v127, 0xffff0000, v47
	v_lshlrev_b32_e32 v128, 16, v48
	v_and_b32_e32 v129, 0xffff0000, v48
	v_lshlrev_b32_e32 v130, 16, v49
	v_and_b32_e32 v131, 0xffff0000, v49
	v_pk_mul_f32 v[116:117], v[114:115], v[116:117] op_sel_hi:[0,1]
	v_pk_mul_f32 v[118:119], v[114:115], v[118:119] op_sel_hi:[0,1]
	v_pk_mul_f32 v[120:121], v[114:115], v[120:121] op_sel_hi:[0,1]
	v_pk_mul_f32 v[122:123], v[114:115], v[122:123] op_sel_hi:[0,1]
	v_pk_mul_f32 v[124:125], v[114:115], v[124:125] op_sel_hi:[0,1]
	v_pk_mul_f32 v[126:127], v[114:115], v[126:127] op_sel_hi:[0,1]
	v_pk_mul_f32 v[128:129], v[114:115], v[128:129] op_sel_hi:[0,1]
	v_pk_mul_f32 v[130:131], v[114:115], v[130:131] op_sel_hi:[0,1]
	v_pk_mul_f32 v[132:133], v[8:9], v[116:117]
	v_pk_mul_f32 v[134:135], v[10:11], v[118:119]
	v_pk_mul_f32 v[136:137], v[12:13], v[120:121]
	v_pk_mul_f32 v[138:139], v[14:15], v[122:123]
	v_pk_mul_f32 v[140:141], v[16:17], v[124:125]
	v_pk_mul_f32 v[142:143], v[18:19], v[126:127]
	v_pk_mul_f32 v[144:145], v[20:21], v[128:129]
	v_pk_mul_f32 v[146:147], v[22:23], v[130:131]
	global_store_dwordx4 v2, v[132:135], s[36:37] offset:0
	global_store_dwordx4 v2, v[136:139], s[36:37] offset:1024
	global_store_dwordx4 v2, v[140:143], s[36:37] offset:2048
	global_store_dwordx4 v2, v[144:147], s[36:37] offset:3072
	s_waitcnt vmcnt(33)
	v_add_f32_dpp v112, v60, v60 quad_perm:[1,0,3,2] row_mask:0xf bank_mask:0xf
	s_mov_b64 s[34:35], s[24:25]
	s_add_u32 s24, s24, s22
	v_add_f32_dpp v112, v112, v112 quad_perm:[2,3,0,1] row_mask:0xf bank_mask:0xf
	s_addc_u32 s25, s25, 0
	s_nop 0
	v_add_f32_dpp v112, v112, v112 row_half_mirror row_mask:0xf bank_mask:0xf
	s_nop 1
	v_add_f32_dpp v112, v112, v112 row_mirror row_mask:0xf bank_mask:0xf
	v_fmamk_f32 v112, v112, 0x3a800000, v5
	v_rsq_f32_e32 v114, v112
	v_lshlrev_b32_e32 v116, 16, v52
	v_and_b32_e32 v117, 0xffff0000, v52
	v_lshlrev_b32_e32 v118, 16, v53
	v_and_b32_e32 v119, 0xffff0000, v53
	v_lshlrev_b32_e32 v120, 16, v54
	v_and_b32_e32 v121, 0xffff0000, v54
	v_lshlrev_b32_e32 v122, 16, v55
	v_and_b32_e32 v123, 0xffff0000, v55
	v_lshlrev_b32_e32 v124, 16, v56
	v_and_b32_e32 v125, 0xffff0000, v56
	v_lshlrev_b32_e32 v126, 16, v57
	v_and_b32_e32 v127, 0xffff0000, v57
	v_lshlrev_b32_e32 v128, 16, v58
	v_and_b32_e32 v129, 0xffff0000, v58
	v_lshlrev_b32_e32 v130, 16, v59
	v_and_b32_e32 v131, 0xffff0000, v59
	v_pk_mul_f32 v[116:117], v[114:115], v[116:117] op_sel_hi:[0,1]
	v_pk_mul_f32 v[118:119], v[114:115], v[118:119] op_sel_hi:[0,1]
	v_pk_mul_f32 v[120:121], v[114:115], v[120:121] op_sel_hi:[0,1]
	v_pk_mul_f32 v[122:123], v[114:115], v[122:123] op_sel_hi:[0,1]
	v_pk_mul_f32 v[124:125], v[114:115], v[124:125] op_sel_hi:[0,1]
	v_pk_mul_f32 v[126:127], v[114:115], v[126:127] op_sel_hi:[0,1]
	v_pk_mul_f32 v[128:129], v[114:115], v[128:129] op_sel_hi:[0,1]
	v_pk_mul_f32 v[130:131], v[114:115], v[130:131] op_sel_hi:[0,1]
	v_pk_mul_f32 v[132:133], v[8:9], v[116:117]
	v_pk_mul_f32 v[134:135], v[10:11], v[118:119]
	v_pk_mul_f32 v[136:137], v[12:13], v[120:121]
	v_pk_mul_f32 v[138:139], v[14:15], v[122:123]
	v_pk_mul_f32 v[140:141], v[16:17], v[124:125]
	v_pk_mul_f32 v[142:143], v[18:19], v[126:127]
	v_pk_mul_f32 v[144:145], v[20:21], v[128:129]
	v_pk_mul_f32 v[146:147], v[22:23], v[130:131]
	global_store_dwordx4 v2, v[132:135], s[34:35] offset:0
	global_store_dwordx4 v2, v[136:139], s[34:35] offset:1024
	global_store_dwordx4 v2, v[140:143], s[34:35] offset:2048
	global_store_dwordx4 v2, v[144:147], s[34:35] offset:3072
	s_waitcnt vmcnt(32)
	v_add_f32_dpp v112, v70, v70 quad_perm:[1,0,3,2] row_mask:0xf bank_mask:0xf
	s_mov_b64 s[36:37], s[24:25]
	s_add_u32 s24, s24, s22
	v_add_f32_dpp v112, v112, v112 quad_perm:[2,3,0,1] row_mask:0xf bank_mask:0xf
	s_addc_u32 s25, s25, 0
	s_nop 0
	v_add_f32_dpp v112, v112, v112 row_half_mirror row_mask:0xf bank_mask:0xf
	s_nop 1
	v_add_f32_dpp v112, v112, v112 row_mirror row_mask:0xf bank_mask:0xf
	v_fmamk_f32 v112, v112, 0x3a800000, v5
	v_rsq_f32_e32 v114, v112
	v_lshlrev_b32_e32 v116, 16, v62
	v_and_b32_e32 v117, 0xffff0000, v62
	v_lshlrev_b32_e32 v118, 16, v63
	v_and_b32_e32 v119, 0xffff0000, v63
	v_lshlrev_b32_e32 v120, 16, v64
	v_and_b32_e32 v121, 0xffff0000, v64
	v_lshlrev_b32_e32 v122, 16, v65
	v_and_b32_e32 v123, 0xffff0000, v65
	v_lshlrev_b32_e32 v124, 16, v66
	v_and_b32_e32 v125, 0xffff0000, v66
	v_lshlrev_b32_e32 v126, 16, v67
	v_and_b32_e32 v127, 0xffff0000, v67
	v_lshlrev_b32_e32 v128, 16, v68
	v_and_b32_e32 v129, 0xffff0000, v68
	v_lshlrev_b32_e32 v130, 16, v69
	v_and_b32_e32 v131, 0xffff0000, v69
	v_pk_mul_f32 v[116:117], v[114:115], v[116:117] op_sel_hi:[0,1]
	v_pk_mul_f32 v[118:119], v[114:115], v[118:119] op_sel_hi:[0,1]
	v_pk_mul_f32 v[120:121], v[114:115], v[120:121] op_sel_hi:[0,1]
	v_pk_mul_f32 v[122:123], v[114:115], v[122:123] op_sel_hi:[0,1]
	v_pk_mul_f32 v[124:125], v[114:115], v[124:125] op_sel_hi:[0,1]
	v_pk_mul_f32 v[126:127], v[114:115], v[126:127] op_sel_hi:[0,1]
	v_pk_mul_f32 v[128:129], v[114:115], v[128:129] op_sel_hi:[0,1]
	v_pk_mul_f32 v[130:131], v[114:115], v[130:131] op_sel_hi:[0,1]
	v_pk_mul_f32 v[132:133], v[8:9], v[116:117]
	v_pk_mul_f32 v[134:135], v[10:11], v[118:119]
	v_pk_mul_f32 v[136:137], v[12:13], v[120:121]
	v_pk_mul_f32 v[138:139], v[14:15], v[122:123]
	v_pk_mul_f32 v[140:141], v[16:17], v[124:125]
	v_pk_mul_f32 v[142:143], v[18:19], v[126:127]
	v_pk_mul_f32 v[144:145], v[20:21], v[128:129]
	v_pk_mul_f32 v[146:147], v[22:23], v[130:131]
	global_store_dwordx4 v2, v[132:135], s[36:37] offset:0
	global_store_dwordx4 v2, v[136:139], s[36:37] offset:1024
	global_store_dwordx4 v2, v[140:143], s[36:37] offset:2048
	global_store_dwordx4 v2, v[144:147], s[36:37] offset:3072
.Lfin_loop:
	s_add_i32 s14, s12, s23
	s_cmp_lt_i32 s14, 0x10000
	s_cbranch_scc0 .Lfin_drain
	s_mov_b64 s[26:27], s[16:17]
	s_mov_b64 s[28:29], s[18:19]
	global_load_dword v40, v4, s[26:27]
	global_load_dwordx2 v[32:33], v3, s[28:29] offset:0
	global_load_dwordx2 v[34:35], v3, s[28:29] offset:512
	global_load_dwordx2 v[36:37], v3, s[28:29] offset:1024
	global_load_dwordx2 v[38:39], v3, s[28:29] offset:1536
	s_add_u32 s16, s16, s20
	s_addc_u32 s17, s17, 0
	s_add_u32 s18, s18, s21
	s_addc_u32 s19, s19, 0
	s_add_i32 s12, s12, s13
	s_mov_b64 s[30:31], s[16:17]
	s_mov_b64 s[32:33], s[18:19]
	global_load_dword v50, v4, s[30:31]
	global_load_dwordx2 v[42:43], v3, s[32:33] offset:0
	global_load_dwordx2 v[44:45], v3, s[32:33] offset:512
	global_load_dwordx2 v[46:47], v3, s[32:33] offset:1024
	global_load_dwordx2 v[48:49], v3, s[32:33] offset:1536
	s_add_u32 s16, s16, s20
	s_addc_u32 s17, s17, 0
	s_add_u32 s18, s18, s21
	s_addc_u32 s19, s19, 0
	s_add_i32 s12, s12, s13
	s_mov_b64 s[26:27], s[16:17]
	s_mov_b64 s[28:29], s[18:19]
	global_load_dword v60, v4, s[26:27]
	global_load_dwordx2 v[52:53], v3, s[28:29] offset:0
	global_load_dwordx2 v[54:55], v3, s[28:29] offset:512
	global_load_dwordx2 v[56:57], v3, s[28:29] offset:1024
	global_load_dwordx2 v[58:59], v3, s[28:29] offset:1536
	s_add_u32 s16, s16, s20
	s_addc_u32 s17, s17, 0
	s_add_u32 s18, s18, s21
	s_addc_u32 s19, s19, 0
	s_add_i32 s12, s12, s13
	s_mov_b64 s[30:31], s[16:17]
	s_mov_b64 s[32:33], s[18:19]
	global_load_dword v70, v4, s[30:31]
	global_load_dwordx2 v[62:63], v3, s[32:33] offset:0
	global_load_dwordx2 v[64:65], v3, s[32:33] offset:512
	global_load_dwordx2 v[66:67], v3, s[32:33] offset:1024
	global_load_dwordx2 v[68:69], v3, s[32:33] offset:1536
	s_add_u32 s16, s16, s20
	s_addc_u32 s17, s17, 0
	s_add_u32 s18, s18, s21
	s_addc_u32 s19, s19, 0
	s_add_i32 s12, s12, s13
	s_waitcnt vmcnt(51)
	v_add_f32_dpp v112, v80, v80 quad_perm:[1,0,3,2] row_mask:0xf bank_mask:0xf
	s_mov_b64 s[34:35], s[24:25]
	s_add_u32 s24, s24, s22
	v_add_f32_dpp v112, v112, v112 quad_perm:[2,3,0,1] row_mask:0xf bank_mask:0xf
	s_addc_u32 s25, s25, 0
	s_nop 0
	v_add_f32_dpp v112, v112, v112 row_half_mirror row_mask:0xf bank_mask:0xf
	s_nop 1
	v_add_f32_dpp v112, v112, v112 row_mirror row_mask:0xf bank_mask:0xf
	v_fmamk_f32 v112, v112, 0x3a800000, v5
	v_rsq_f32_e32 v114, v112
	v_lshlrev_b32_e32 v116, 16, v72
	v_and_b32_e32 v117, 0xffff0000, v72
	v_lshlrev_b32_e32 v118, 16, v73
	v_and_b32_e32 v119, 0xffff0000, v73
	v_lshlrev_b32_e32 v120, 16, v74
	v_and_b32_e32 v121, 0xffff0000, v74
	v_lshlrev_b32_e32 v122, 16, v75
	v_and_b32_e32 v123, 0xffff0000, v75
	v_lshlrev_b32_e32 v124, 16, v76
	v_and_b32_e32 v125, 0xffff0000, v76
	v_lshlrev_b32_e32 v126, 16, v77
	v_and_b32_e32 v127, 0xffff0000, v77
	v_lshlrev_b32_e32 v128, 16, v78
	v_and_b32_e32 v129, 0xffff0000, v78
	v_lshlrev_b32_e32 v130, 16, v79
	v_and_b32_e32 v131, 0xffff0000, v79
	v_pk_mul_f32 v[116:117], v[114:115], v[116:117] op_sel_hi:[0,1]
	v_pk_mul_f32 v[118:119], v[114:115], v[118:119] op_sel_hi:[0,1]
	v_pk_mul_f32 v[120:121], v[114:115], v[120:121] op_sel_hi:[0,1]
	v_pk_mul_f32 v[122:123], v[114:115], v[122:123] op_sel_hi:[0,1]
	v_pk_mul_f32 v[124:125], v[114:115], v[124:125] op_sel_hi:[0,1]
	v_pk_mul_f32 v[126:127], v[114:115], v[126:127] op_sel_hi:[0,1]
	v_pk_mul_f32 v[128:129], v[114:115], v[128:129] op_sel_hi:[0,1]
	v_pk_mul_f32 v[130:131], v[114:115], v[130:131] op_sel_hi:[0,1]
	v_pk_mul_f32 v[132:133], v[8:9], v[116:117]
	v_pk_mul_f32 v[134:135], v[10:11], v[118:119]
	v_pk_mul_f32 v[136:137], v[12:13], v[120:121]
	v_pk_mul_f32 v[138:139], v[14:15], v[122:123]
	v_pk_mul_f32 v[140:141], v[16:17], v[124:125]
	v_pk_mul_f32 v[142:143], v[18:19], v[126:127]
	v_pk_mul_f32 v[144:145], v[20:21], v[128:129]
	v_pk_mul_f32 v[146:147], v[22:23], v[130:131]
	global_store_dwordx4 v2, v[132:135], s[34:35] offset:0
	global_store_dwordx4 v2, v[136:139], s[34:35] offset:1024
	global_store_dwordx4 v2, v[140:143], s[34:35] offset:2048
	global_store_dwordx4 v2, v[144:147], s[34:35] offset:3072
	s_waitcnt vmcnt(50)
	v_add_f32_dpp v112, v90, v90 quad_perm:[1,0,3,2] row_mask:0xf bank_mask:0xf
	s_mov_b64 s[36:37], s[24:25]
	s_add_u32 s24, s24, s22
	v_add_f32_dpp v112, v112, v112 quad_perm:[2,3,0,1] row_mask:0xf bank_mask:0xf
	s_addc_u32 s25, s25, 0
	s_nop 0
	v_add_f32_dpp v112, v112, v112 row_half_mirror row_mask:0xf bank_mask:0xf
	s_nop 1
	v_add_f32_dpp v112, v112, v112 row_mirror row_mask:0xf bank_mask:0xf
	v_fmamk_f32 v112, v112, 0x3a800000, v5
	v_rsq_f32_e32 v114, v112
	v_lshlrev_b32_e32 v116, 16, v82
	v_and_b32_e32 v117, 0xffff0000, v82
	v_lshlrev_b32_e32 v118, 16, v83
	v_and_b32_e32 v119, 0xffff0000, v83
	v_lshlrev_b32_e32 v120, 16, v84
	v_and_b32_e32 v121, 0xffff0000, v84
	v_lshlrev_b32_e32 v122, 16, v85
	v_and_b32_e32 v123, 0xffff0000, v85
	v_lshlrev_b32_e32 v124, 16, v86
	v_and_b32_e32 v125, 0xffff0000, v86
	v_lshlrev_b32_e32 v126, 16, v87
	v_and_b32_e32 v127, 0xffff0000, v87
	v_lshlrev_b32_e32 v128, 16, v88
	v_and_b32_e32 v129, 0xffff0000, v88
	v_lshlrev_b32_e32 v130, 16, v89
	v_and_b32_e32 v131, 0xffff0000, v89
	v_pk_mul_f32 v[116:117], v[114:115], v[116:117] op_sel_hi:[0,1]
	v_pk_mul_f32 v[118:119], v[114:115], v[118:119] op_sel_hi:[0,1]
	v_pk_mul_f32 v[120:121], v[114:115], v[120:121] op_sel_hi:[0,1]
	v_pk_mul_f32 v[122:123], v[114:115], v[122:123] op_sel_hi:[0,1]
	v_pk_mul_f32 v[124:125], v[114:115], v[124:125] op_sel_hi:[0,1]
	v_pk_mul_f32 v[126:127], v[114:115], v[126:127] op_sel_hi:[0,1]
	v_pk_mul_f32 v[128:129], v[114:115], v[128:129] op_sel_hi:[0,1]
	v_pk_mul_f32 v[130:131], v[114:115], v[130:131] op_sel_hi:[0,1]
	v_pk_mul_f32 v[132:133], v[8:9], v[116:117]
	v_pk_mul_f32 v[134:135], v[10:11], v[118:119]
	v_pk_mul_f32 v[136:137], v[12:13], v[120:121]
	v_pk_mul_f32 v[138:139], v[14:15], v[122:123]
	v_pk_mul_f32 v[140:141], v[16:17], v[124:125]
	v_pk_mul_f32 v[142:143], v[18:19], v[126:127]
	v_pk_mul_f32 v[144:145], v[20:21], v[128:129]
	v_pk_mul_f32 v[146:147], v[22:23], v[130:131]
	global_store_dwordx4 v2, v[132:135], s[36:37] offset:0
	global_store_dwordx4 v2, v[136:139], s[36:37] offset:1024
	global_store_dwordx4 v2, v[140:143], s[36:37] offset:2048
	global_store_dwordx4 v2, v[144:147], s[36:37] offset:3072
	s_waitcnt vmcnt(49)
	v_add_f32_dpp v112, v100, v100 quad_perm:[1,0,3,2] row_mask:0xf bank_mask:0xf
	s_mov_b64 s[34:35], s[24:25]
	s_add_u32 s24, s24, s22
	v_add_f32_dpp v112, v112, v112 quad_perm:[2,3,0,1] row_mask:0xf bank_mask:0xf
	s_addc_u32 s25, s25, 0
	s_nop 0
	v_add_f32_dpp v112, v112, v112 row_half_mirror row_mask:0xf bank_mask:0xf
	s_nop 1
	v_add_f32_dpp v112, v112, v112 row_mirror row_mask:0xf bank_mask:0xf
	v_fmamk_f32 v112, v112, 0x3a800000, v5
	v_rsq_f32_e32 v114, v112
	v_lshlrev_b32_e32 v116, 16, v92
	v_and_b32_e32 v117, 0xffff0000, v92
	v_lshlrev_b32_e32 v118, 16, v93
	v_and_b32_e32 v119, 0xffff0000, v93
	v_lshlrev_b32_e32 v120, 16, v94
	v_and_b32_e32 v121, 0xffff0000, v94
	v_lshlrev_b32_e32 v122, 16, v95
	v_and_b32_e32 v123, 0xffff0000, v95
	v_lshlrev_b32_e32 v124, 16, v96
	v_and_b32_e32 v125, 0xffff0000, v96
	v_lshlrev_b32_e32 v126, 16, v97
	v_and_b32_e32 v127, 0xffff0000, v97
	v_lshlrev_b32_e32 v128, 16, v98
	v_and_b32_e32 v129, 0xffff0000, v98
	v_lshlrev_b32_e32 v130, 16, v99
	v_and_b32_e32 v131, 0xffff0000, v99
	v_pk_mul_f32 v[116:117], v[114:115], v[116:117] op_sel_hi:[0,1]
	v_pk_mul_f32 v[118:119], v[114:115], v[118:119] op_sel_hi:[0,1]
	v_pk_mul_f32 v[120:121], v[114:115], v[120:121] op_sel_hi:[0,1]
	v_pk_mul_f32 v[122:123], v[114:115], v[122:123] op_sel_hi:[0,1]
	v_pk_mul_f32 v[124:125], v[114:115], v[124:125] op_sel_hi:[0,1]
	v_pk_mul_f32 v[126:127], v[114:115], v[126:127] op_sel_hi:[0,1]
	v_pk_mul_f32 v[128:129], v[114:115], v[128:129] op_sel_hi:[0,1]
	v_pk_mul_f32 v[130:131], v[114:115], v[130:131] op_sel_hi:[0,1]
	v_pk_mul_f32 v[132:133], v[8:9], v[116:117]
	v_pk_mul_f32 v[134:135], v[10:11], v[118:119]
	v_pk_mul_f32 v[136:137], v[12:13], v[120:121]
	v_pk_mul_f32 v[138:139], v[14:15], v[122:123]
	v_pk_mul_f32 v[140:141], v[16:17], v[124:125]
	v_pk_mul_f32 v[142:143], v[18:19], v[126:127]
	v_pk_mul_f32 v[144:145], v[20:21], v[128:129]
	v_pk_mul_f32 v[146:147], v[22:23], v[130:131]
	global_store_dwordx4 v2, v[132:135], s[34:35] offset:0
	global_store_dwordx4 v2, v[136:139], s[34:35] offset:1024
	global_store_dwordx4 v2, v[140:143], s[34:35] offset:2048
	global_store_dwordx4 v2, v[144:147], s[34:35] offset:3072
	s_waitcnt vmcnt(48)
	v_add_f32_dpp v112, v110, v110 quad_perm:[1,0,3,2] row_mask:0xf bank_mask:0xf
	s_mov_b64 s[36:37], s[24:25]
	s_add_u32 s24, s24, s22
	v_add_f32_dpp v112, v112, v112 quad_perm:[2,3,0,1] row_mask:0xf bank_mask:0xf
	s_addc_u32 s25, s25, 0
	s_nop 0
	v_add_f32_dpp v112, v112, v112 row_half_mirror row_mask:0xf bank_mask:0xf
	s_nop 1
	v_add_f32_dpp v112, v112, v112 row_mirror row_mask:0xf bank_mask:0xf
	v_fmamk_f32 v112, v112, 0x3a800000, v5
	v_rsq_f32_e32 v114, v112
	v_lshlrev_b32_e32 v116, 16, v102
	v_and_b32_e32 v117, 0xffff0000, v102
	v_lshlrev_b32_e32 v118, 16, v103
	v_and_b32_e32 v119, 0xffff0000, v103
	v_lshlrev_b32_e32 v120, 16, v104
	v_and_b32_e32 v121, 0xffff0000, v104
	v_lshlrev_b32_e32 v122, 16, v105
	v_and_b32_e32 v123, 0xffff0000, v105
	v_lshlrev_b32_e32 v124, 16, v106
	v_and_b32_e32 v125, 0xffff0000, v106
	v_lshlrev_b32_e32 v126, 16, v107
	v_and_b32_e32 v127, 0xffff0000, v107
	v_lshlrev_b32_e32 v128, 16, v108
	v_and_b32_e32 v129, 0xffff0000, v108
	v_lshlrev_b32_e32 v130, 16, v109
	v_and_b32_e32 v131, 0xffff0000, v109
	v_pk_mul_f32 v[116:117], v[114:115], v[116:117] op_sel_hi:[0,1]
	v_pk_mul_f32 v[118:119], v[114:115], v[118:119] op_sel_hi:[0,1]
	v_pk_mul_f32 v[120:121], v[114:115], v[120:121] op_sel_hi:[0,1]
	v_pk_mul_f32 v[122:123], v[114:115], v[122:123] op_sel_hi:[0,1]
	v_pk_mul_f32 v[124:125], v[114:115], v[124:125] op_sel_hi:[0,1]
	v_pk_mul_f32 v[126:127], v[114:115], v[126:127] op_sel_hi:[0,1]
	v_pk_mul_f32 v[128:129], v[114:115], v[128:129] op_sel_hi:[0,1]
	v_pk_mul_f32 v[130:131], v[114:115], v[130:131] op_sel_hi:[0,1]
	v_pk_mul_f32 v[132:133], v[8:9], v[116:117]
	v_pk_mul_f32 v[134:135], v[10:11], v[118:119]
	v_pk_mul_f32 v[136:137], v[12:13], v[120:121]
	v_pk_mul_f32 v[138:139], v[14:15], v[122:123]
	v_pk_mul_f32 v[140:141], v[16:17], v[124:125]
	v_pk_mul_f32 v[142:143], v[18:19], v[126:127]
	v_pk_mul_f32 v[144:145], v[20:21], v[128:129]
	v_pk_mul_f32 v[146:147], v[22:23], v[130:131]
	global_store_dwordx4 v2, v[132:135], s[36:37] offset:0
	global_store_dwordx4 v2, v[136:139], s[36:37] offset:1024
	global_store_dwordx4 v2, v[140:143], s[36:37] offset:2048
	global_store_dwordx4 v2, v[144:147], s[36:37] offset:3072
	s_mov_b64 s[26:27], s[16:17]
	s_mov_b64 s[28:29], s[18:19]
	global_load_dword v80, v4, s[26:27]
	global_load_dwordx2 v[72:73], v3, s[28:29] offset:0
	global_load_dwordx2 v[74:75], v3, s[28:29] offset:512
	global_load_dwordx2 v[76:77], v3, s[28:29] offset:1024
	global_load_dwordx2 v[78:79], v3, s[28:29] offset:1536
	s_add_u32 s16, s16, s20
	s_addc_u32 s17, s17, 0
	s_add_u32 s18, s18, s21
	s_addc_u32 s19, s19, 0
	s_add_i32 s12, s12, s13
	s_mov_b64 s[30:31], s[16:17]
	s_mov_b64 s[32:33], s[18:19]
	global_load_dword v90, v4, s[30:31]
	global_load_dwordx2 v[82:83], v3, s[32:33] offset:0
	global_load_dwordx2 v[84:85], v3, s[32:33] offset:512
	global_load_dwordx2 v[86:87], v3, s[32:33] offset:1024
	global_load_dwordx2 v[88:89], v3, s[32:33] offset:1536
	s_add_u32 s16, s16, s20
	s_addc_u32 s17, s17, 0
	s_add_u32 s18, s18, s21
	s_addc_u32 s19, s19, 0
	s_add_i32 s12, s12, s13
	s_mov_b64 s[26:27], s[16:17]
	s_mov_b64 s[28:29], s[18:19]
	global_load_dword v100, v4, s[26:27]
	global_load_dwordx2 v[92:93], v3, s[28:29] offset:0
	global_load_dwordx2 v[94:95], v3, s[28:29] offset:512
	global_load_dwordx2 v[96:97], v3, s[28:29] offset:1024
	global_load_dwordx2 v[98:99], v3, s[28:29] offset:1536
	s_add_u32 s16, s16, s20
	s_addc_u32 s17, s17, 0
	s_add_u32 s18, s18, s21
	s_addc_u32 s19, s19, 0
	s_add_i32 s12, s12, s13
	s_mov_b64 s[30:31], s[16:17]
	s_mov_b64 s[32:33], s[18:19]
	global_load_dword v110, v4, s[30:31]
	global_load_dwordx2 v[102:103], v3, s[32:33] offset:0
	global_load_dwordx2 v[104:105], v3, s[32:33] offset:512
	global_load_dwordx2 v[106:107], v3, s[32:33] offset:1024
	global_load_dwordx2 v[108:109], v3, s[32:33] offset:1536
	s_add_u32 s16, s16, s20
	s_addc_u32 s17, s17, 0
	s_add_u32 s18, s18, s21
	s_addc_u32 s19, s19, 0
	s_add_i32 s12, s12, s13
	s_waitcnt vmcnt(51)
	v_add_f32_dpp v112, v40, v40 quad_perm:[1,0,3,2] row_mask:0xf bank_mask:0xf
	s_mov_b64 s[34:35], s[24:25]
	s_add_u32 s24, s24, s22
	v_add_f32_dpp v112, v112, v112 quad_perm:[2,3,0,1] row_mask:0xf bank_mask:0xf
	s_addc_u32 s25, s25, 0
	s_nop 0
	v_add_f32_dpp v112, v112, v112 row_half_mirror row_mask:0xf bank_mask:0xf
	s_nop 1
	v_add_f32_dpp v112, v112, v112 row_mirror row_mask:0xf bank_mask:0xf
	v_fmamk_f32 v112, v112, 0x3a800000, v5
	v_rsq_f32_e32 v114, v112
	v_lshlrev_b32_e32 v116, 16, v32
	v_and_b32_e32 v117, 0xffff0000, v32
	v_lshlrev_b32_e32 v118, 16, v33
	v_and_b32_e32 v119, 0xffff0000, v33
	v_lshlrev_b32_e32 v120, 16, v34
	v_and_b32_e32 v121, 0xffff0000, v34
	v_lshlrev_b32_e32 v122, 16, v35
	v_and_b32_e32 v123, 0xffff0000, v35
	v_lshlrev_b32_e32 v124, 16, v36
	v_and_b32_e32 v125, 0xffff0000, v36
	v_lshlrev_b32_e32 v126, 16, v37
	v_and_b32_e32 v127, 0xffff0000, v37
	v_lshlrev_b32_e32 v128, 16, v38
	v_and_b32_e32 v129, 0xffff0000, v38
	v_lshlrev_b32_e32 v130, 16, v39
	v_and_b32_e32 v131, 0xffff0000, v39
	v_pk_mul_f32 v[116:117], v[114:115], v[116:117] op_sel_hi:[0,1]
	v_pk_mul_f32 v[118:119], v[114:115], v[118:119] op_sel_hi:[0,1]
	v_pk_mul_f32 v[120:121], v[114:115], v[120:121] op_sel_hi:[0,1]
	v_pk_mul_f32 v[122:123], v[114:115], v[122:123] op_sel_hi:[0,1]
	v_pk_mul_f32 v[124:125], v[114:115], v[124:125] op_sel_hi:[0,1]
	v_pk_mul_f32 v[126:127], v[114:115], v[126:127] op_sel_hi:[0,1]
	v_pk_mul_f32 v[128:129], v[114:115], v[128:129] op_sel_hi:[0,1]
	v_pk_mul_f32 v[130:131], v[114:115], v[130:131] op_sel_hi:[0,1]
	v_pk_mul_f32 v[132:133], v[8:9], v[116:117]
	v_pk_mul_f32 v[134:135], v[10:11], v[118:119]
	v_pk_mul_f32 v[136:137], v[12:13], v[120:121]
	v_pk_mul_f32 v[138:139], v[14:15], v[122:123]
	v_pk_mul_f32 v[140:141], v[16:17], v[124:125]
	v_pk_mul_f32 v[142:143], v[18:19], v[126:127]
	v_pk_mul_f32 v[144:145], v[20:21], v[128:129]
	v_pk_mul_f32 v[146:147], v[22:23], v[130:131]
	global_store_dwordx4 v2, v[132:135], s[34:35] offset:0
	global_store_dwordx4 v2, v[136:139], s[34:35] offset:1024
	global_store_dwordx4 v2, v[140:143], s[34:35] offset:2048
	global_store_dwordx4 v2, v[144:147], s[34:35] offset:3072
	s_waitcnt vmcnt(50)
	v_add_f32_dpp v112, v50, v50 quad_perm:[1,0,3,2] row_mask:0xf bank_mask:0xf
	s_mov_b64 s[36:37], s[24:25]
	s_add_u32 s24, s24, s22
	v_add_f32_dpp v112, v112, v112 quad_perm:[2,3,0,1] row_mask:0xf bank_mask:0xf
	s_addc_u32 s25, s25, 0
	s_nop 0
	v_add_f32_dpp v112, v112, v112 row_half_mirror row_mask:0xf bank_mask:0xf
	s_nop 1
	v_add_f32_dpp v112, v112, v112 row_mirror row_mask:0xf bank_mask:0xf
	v_fmamk_f32 v112, v112, 0x3a800000, v5
	v_rsq_f32_e32 v114, v112
	v_lshlrev_b32_e32 v116, 16, v42
	v_and_b32_e32 v117, 0xffff0000, v42
	v_lshlrev_b32_e32 v118, 16, v43
	v_and_b32_e32 v119, 0xffff0000, v43
	v_lshlrev_b32_e32 v120, 16, v44
	v_and_b32_e32 v121, 0xffff0000, v44
	v_lshlrev_b32_e32 v122, 16, v45
	v_and_b32_e32 v123, 0xffff0000, v45
	v_lshlrev_b32_e32 v124, 16, v46
	v_and_b32_e32 v125, 0xffff0000, v46
	v_lshlrev_b32_e32 v126, 16, v47
	v_and_b32_e32 v127, 0xffff0000, v47
	v_lshlrev_b32_e32 v128, 16, v48
	v_and_b32_e32 v129, 0xffff0000, v48
	v_lshlrev_b32_e32 v130, 16, v49
	v_and_b32_e32 v131, 0xffff0000, v49
	v_pk_mul_f32 v[116:117], v[114:115], v[116:117] op_sel_hi:[0,1]
	v_pk_mul_f32 v[118:119], v[114:115], v[118:119] op_sel_hi:[0,1]
	v_pk_mul_f32 v[120:121], v[114:115], v[120:121] op_sel_hi:[0,1]
	v_pk_mul_f32 v[122:123], v[114:115], v[122:123] op_sel_hi:[0,1]
	v_pk_mul_f32 v[124:125], v[114:115], v[124:125] op_sel_hi:[0,1]
	v_pk_mul_f32 v[126:127], v[114:115], v[126:127] op_sel_hi:[0,1]
	v_pk_mul_f32 v[128:129], v[114:115], v[128:129] op_sel_hi:[0,1]
	v_pk_mul_f32 v[130:131], v[114:115], v[130:131] op_sel_hi:[0,1]
	v_pk_mul_f32 v[132:133], v[8:9], v[116:117]
	v_pk_mul_f32 v[134:135], v[10:11], v[118:119]
	v_pk_mul_f32 v[136:137], v[12:13], v[120:121]
	v_pk_mul_f32 v[138:139], v[14:15], v[122:123]
	v_pk_mul_f32 v[140:141], v[16:17], v[124:125]
	v_pk_mul_f32 v[142:143], v[18:19], v[126:127]
	v_pk_mul_f32 v[144:145], v[20:21], v[128:129]
	v_pk_mul_f32 v[146:147], v[22:23], v[130:131]
	global_store_dwordx4 v2, v[132:135], s[36:37] offset:0
	global_store_dwordx4 v2, v[136:139], s[36:37] offset:1024
	global_store_dwordx4 v2, v[140:143], s[36:37] offset:2048
	global_store_dwordx4 v2, v[144:147], s[36:37] offset:3072
	s_waitcnt vmcnt(49)
	v_add_f32_dpp v112, v60, v60 quad_perm:[1,0,3,2] row_mask:0xf bank_mask:0xf
	s_mov_b64 s[34:35], s[24:25]
	s_add_u32 s24, s24, s22
	v_add_f32_dpp v112, v112, v112 quad_perm:[2,3,0,1] row_mask:0xf bank_mask:0xf
	s_addc_u32 s25, s25, 0
	s_nop 0
	v_add_f32_dpp v112, v112, v112 row_half_mirror row_mask:0xf bank_mask:0xf
	s_nop 1
	v_add_f32_dpp v112, v112, v112 row_mirror row_mask:0xf bank_mask:0xf
	v_fmamk_f32 v112, v112, 0x3a800000, v5
	v_rsq_f32_e32 v114, v112
	v_lshlrev_b32_e32 v116, 16, v52
	v_and_b32_e32 v117, 0xffff0000, v52
	v_lshlrev_b32_e32 v118, 16, v53
	v_and_b32_e32 v119, 0xffff0000, v53
	v_lshlrev_b32_e32 v120, 16, v54
	v_and_b32_e32 v121, 0xffff0000, v54
	v_lshlrev_b32_e32 v122, 16, v55
	v_and_b32_e32 v123, 0xffff0000, v55
	v_lshlrev_b32_e32 v124, 16, v56
	v_and_b32_e32 v125, 0xffff0000, v56
	v_lshlrev_b32_e32 v126, 16, v57
	v_and_b32_e32 v127, 0xffff0000, v57
	v_lshlrev_b32_e32 v128, 16, v58
	v_and_b32_e32 v129, 0xffff0000, v58
	v_lshlrev_b32_e32 v130, 16, v59
	v_and_b32_e32 v131, 0xffff0000, v59
	v_pk_mul_f32 v[116:117], v[114:115], v[116:117] op_sel_hi:[0,1]
	v_pk_mul_f32 v[118:119], v[114:115], v[118:119] op_sel_hi:[0,1]
	v_pk_mul_f32 v[120:121], v[114:115], v[120:121] op_sel_hi:[0,1]
	v_pk_mul_f32 v[122:123], v[114:115], v[122:123] op_sel_hi:[0,1]
	v_pk_mul_f32 v[124:125], v[114:115], v[124:125] op_sel_hi:[0,1]
	v_pk_mul_f32 v[126:127], v[114:115], v[126:127] op_sel_hi:[0,1]
	v_pk_mul_f32 v[128:129], v[114:115], v[128:129] op_sel_hi:[0,1]
	v_pk_mul_f32 v[130:131], v[114:115], v[130:131] op_sel_hi:[0,1]
	v_pk_mul_f32 v[132:133], v[8:9], v[116:117]
	v_pk_mul_f32 v[134:135], v[10:11], v[118:119]
	v_pk_mul_f32 v[136:137], v[12:13], v[120:121]
	v_pk_mul_f32 v[138:139], v[14:15], v[122:123]
	v_pk_mul_f32 v[140:141], v[16:17], v[124:125]
	v_pk_mul_f32 v[142:143], v[18:19], v[126:127]
	v_pk_mul_f32 v[144:145], v[20:21], v[128:129]
	v_pk_mul_f32 v[146:147], v[22:23], v[130:131]
	global_store_dwordx4 v2, v[132:135], s[34:35] offset:0
	global_store_dwordx4 v2, v[136:139], s[34:35] offset:1024
	global_store_dwordx4 v2, v[140:143], s[34:35] offset:2048
	global_store_dwordx4 v2, v[144:147], s[34:35] offset:3072
	s_waitcnt vmcnt(48)
	v_add_f32_dpp v112, v70, v70 quad_perm:[1,0,3,2] row_mask:0xf bank_mask:0xf
	s_mov_b64 s[36:37], s[24:25]
	s_add_u32 s24, s24, s22
	v_add_f32_dpp v112, v112, v112 quad_perm:[2,3,0,1] row_mask:0xf bank_mask:0xf
	s_addc_u32 s25, s25, 0
	s_nop 0
	v_add_f32_dpp v112, v112, v112 row_half_mirror row_mask:0xf bank_mask:0xf
	s_nop 1
	v_add_f32_dpp v112, v112, v112 row_mirror row_mask:0xf bank_mask:0xf
	v_fmamk_f32 v112, v112, 0x3a800000, v5
	v_rsq_f32_e32 v114, v112
	v_lshlrev_b32_e32 v116, 16, v62
	v_and_b32_e32 v117, 0xffff0000, v62
	v_lshlrev_b32_e32 v118, 16, v63
	v_and_b32_e32 v119, 0xffff0000, v63
	v_lshlrev_b32_e32 v120, 16, v64
	v_and_b32_e32 v121, 0xffff0000, v64
	v_lshlrev_b32_e32 v122, 16, v65
	v_and_b32_e32 v123, 0xffff0000, v65
	v_lshlrev_b32_e32 v124, 16, v66
	v_and_b32_e32 v125, 0xffff0000, v66
	v_lshlrev_b32_e32 v126, 16, v67
	v_and_b32_e32 v127, 0xffff0000, v67
	v_lshlrev_b32_e32 v128, 16, v68
	v_and_b32_e32 v129, 0xffff0000, v68
	v_lshlrev_b32_e32 v130, 16, v69
	v_and_b32_e32 v131, 0xffff0000, v69
	v_pk_mul_f32 v[116:117], v[114:115], v[116:117] op_sel_hi:[0,1]
	v_pk_mul_f32 v[118:119], v[114:115], v[118:119] op_sel_hi:[0,1]
	v_pk_mul_f32 v[120:121], v[114:115], v[120:121] op_sel_hi:[0,1]
	v_pk_mul_f32 v[122:123], v[114:115], v[122:123] op_sel_hi:[0,1]
	v_pk_mul_f32 v[124:125], v[114:115], v[124:125] op_sel_hi:[0,1]
	v_pk_mul_f32 v[126:127], v[114:115], v[126:127] op_sel_hi:[0,1]
	v_pk_mul_f32 v[128:129], v[114:115], v[128:129] op_sel_hi:[0,1]
	v_pk_mul_f32 v[130:131], v[114:115], v[130:131] op_sel_hi:[0,1]
	v_pk_mul_f32 v[132:133], v[8:9], v[116:117]
	v_pk_mul_f32 v[134:135], v[10:11], v[118:119]
	v_pk_mul_f32 v[136:137], v[12:13], v[120:121]
	v_pk_mul_f32 v[138:139], v[14:15], v[122:123]
	v_pk_mul_f32 v[140:141], v[16:17], v[124:125]
	v_pk_mul_f32 v[142:143], v[18:19], v[126:127]
	v_pk_mul_f32 v[144:145], v[20:21], v[128:129]
	v_pk_mul_f32 v[146:147], v[22:23], v[130:131]
	global_store_dwordx4 v2, v[132:135], s[36:37] offset:0
	global_store_dwordx4 v2, v[136:139], s[36:37] offset:1024
	global_store_dwordx4 v2, v[140:143], s[36:37] offset:2048
	global_store_dwordx4 v2, v[144:147], s[36:37] offset:3072
	s_branch .Lfin_loop
.Lfin_drain:
	s_waitcnt vmcnt(31)
	v_add_f32_dpp v112, v80, v80 quad_perm:[1,0,3,2] row_mask:0xf bank_mask:0xf
	s_mov_b64 s[34:35], s[24:25]
	s_add_u32 s24, s24, s22
	v_add_f32_dpp v112, v112, v112 quad_perm:[2,3,0,1] row_mask:0xf bank_mask:0xf
	s_addc_u32 s25, s25, 0
	s_nop 0
	v_add_f32_dpp v112, v112, v112 row_half_mirror row_mask:0xf bank_mask:0xf
	s_nop 1
	v_add_f32_dpp v112, v112, v112 row_mirror row_mask:0xf bank_mask:0xf
	v_fmamk_f32 v112, v112, 0x3a800000, v5
	v_rsq_f32_e32 v114, v112
	v_lshlrev_b32_e32 v116, 16, v72
	v_and_b32_e32 v117, 0xffff0000, v72
	v_lshlrev_b32_e32 v118, 16, v73
	v_and_b32_e32 v119, 0xffff0000, v73
	v_lshlrev_b32_e32 v120, 16, v74
	v_and_b32_e32 v121, 0xffff0000, v74
	v_lshlrev_b32_e32 v122, 16, v75
	v_and_b32_e32 v123, 0xffff0000, v75
	v_lshlrev_b32_e32 v124, 16, v76
	v_and_b32_e32 v125, 0xffff0000, v76
	v_lshlrev_b32_e32 v126, 16, v77
	v_and_b32_e32 v127, 0xffff0000, v77
	v_lshlrev_b32_e32 v128, 16, v78
	v_and_b32_e32 v129, 0xffff0000, v78
	v_lshlrev_b32_e32 v130, 16, v79
	v_and_b32_e32 v131, 0xffff0000, v79
	v_pk_mul_f32 v[116:117], v[114:115], v[116:117] op_sel_hi:[0,1]
	v_pk_mul_f32 v[118:119], v[114:115], v[118:119] op_sel_hi:[0,1]
	v_pk_mul_f32 v[120:121], v[114:115], v[120:121] op_sel_hi:[0,1]
	v_pk_mul_f32 v[122:123], v[114:115], v[122:123] op_sel_hi:[0,1]
	v_pk_mul_f32 v[124:125], v[114:115], v[124:125] op_sel_hi:[0,1]
	v_pk_mul_f32 v[126:127], v[114:115], v[126:127] op_sel_hi:[0,1]
	v_pk_mul_f32 v[128:129], v[114:115], v[128:129] op_sel_hi:[0,1]
	v_pk_mul_f32 v[130:131], v[114:115], v[130:131] op_sel_hi:[0,1]
	v_pk_mul_f32 v[132:133], v[8:9], v[116:117]
	v_pk_mul_f32 v[134:135], v[10:11], v[118:119]
	v_pk_mul_f32 v[136:137], v[12:13], v[120:121]
	v_pk_mul_f32 v[138:139], v[14:15], v[122:123]
	v_pk_mul_f32 v[140:141], v[16:17], v[124:125]
	v_pk_mul_f32 v[142:143], v[18:19], v[126:127]
	v_pk_mul_f32 v[144:145], v[20:21], v[128:129]
	v_pk_mul_f32 v[146:147], v[22:23], v[130:131]
	global_store_dwordx4 v2, v[132:135], s[34:35] offset:0
	global_store_dwordx4 v2, v[136:139], s[34:35] offset:1024
	global_store_dwordx4 v2, v[140:143], s[34:35] offset:2048
	global_store_dwordx4 v2, v[144:147], s[34:35] offset:3072
	s_waitcnt vmcnt(30)
	v_add_f32_dpp v112, v90, v90 quad_perm:[1,0,3,2] row_mask:0xf bank_mask:0xf
	s_mov_b64 s[36:37], s[24:25]
	s_add_u32 s24, s24, s22
	v_add_f32_dpp v112, v112, v112 quad_perm:[2,3,0,1] row_mask:0xf bank_mask:0xf
	s_addc_u32 s25, s25, 0
	s_nop 0
	v_add_f32_dpp v112, v112, v112 row_half_mirror row_mask:0xf bank_mask:0xf
	s_nop 1
	v_add_f32_dpp v112, v112, v112 row_mirror row_mask:0xf bank_mask:0xf
	v_fmamk_f32 v112, v112, 0x3a800000, v5
	v_rsq_f32_e32 v114, v112
	v_lshlrev_b32_e32 v116, 16, v82
	v_and_b32_e32 v117, 0xffff0000, v82
	v_lshlrev_b32_e32 v118, 16, v83
	v_and_b32_e32 v119, 0xffff0000, v83
	v_lshlrev_b32_e32 v120, 16, v84
	v_and_b32_e32 v121, 0xffff0000, v84
	v_lshlrev_b32_e32 v122, 16, v85
	v_and_b32_e32 v123, 0xffff0000, v85
	v_lshlrev_b32_e32 v124, 16, v86
	v_and_b32_e32 v125, 0xffff0000, v86
	v_lshlrev_b32_e32 v126, 16, v87
	v_and_b32_e32 v127, 0xffff0000, v87
	v_lshlrev_b32_e32 v128, 16, v88
	v_and_b32_e32 v129, 0xffff0000, v88
	v_lshlrev_b32_e32 v130, 16, v89
	v_and_b32_e32 v131, 0xffff0000, v89
	v_pk_mul_f32 v[116:117], v[114:115], v[116:117] op_sel_hi:[0,1]
	v_pk_mul_f32 v[118:119], v[114:115], v[118:119] op_sel_hi:[0,1]
	v_pk_mul_f32 v[120:121], v[114:115], v[120:121] op_sel_hi:[0,1]
	v_pk_mul_f32 v[122:123], v[114:115], v[122:123] op_sel_hi:[0,1]
	v_pk_mul_f32 v[124:125], v[114:115], v[124:125] op_sel_hi:[0,1]
	v_pk_mul_f32 v[126:127], v[114:115], v[126:127] op_sel_hi:[0,1]
	v_pk_mul_f32 v[128:129], v[114:115], v[128:129] op_sel_hi:[0,1]
	v_pk_mul_f32 v[130:131], v[114:115], v[130:131] op_sel_hi:[0,1]
	v_pk_mul_f32 v[132:133], v[8:9], v[116:117]
	v_pk_mul_f32 v[134:135], v[10:11], v[118:119]
	v_pk_mul_f32 v[136:137], v[12:13], v[120:121]
	v_pk_mul_f32 v[138:139], v[14:15], v[122:123]
	v_pk_mul_f32 v[140:141], v[16:17], v[124:125]
	v_pk_mul_f32 v[142:143], v[18:19], v[126:127]
	v_pk_mul_f32 v[144:145], v[20:21], v[128:129]
	v_pk_mul_f32 v[146:147], v[22:23], v[130:131]
	global_store_dwordx4 v2, v[132:135], s[36:37] offset:0
	global_store_dwordx4 v2, v[136:139], s[36:37] offset:1024
	global_store_dwordx4 v2, v[140:143], s[36:37] offset:2048
	global_store_dwordx4 v2, v[144:147], s[36:37] offset:3072
	s_waitcnt vmcnt(29)
	v_add_f32_dpp v112, v100, v100 quad_perm:[1,0,3,2] row_mask:0xf bank_mask:0xf
	s_mov_b64 s[34:35], s[24:25]
	s_add_u32 s24, s24, s22
	v_add_f32_dpp v112, v112, v112 quad_perm:[2,3,0,1] row_mask:0xf bank_mask:0xf
	s_addc_u32 s25, s25, 0
	s_nop 0
	v_add_f32_dpp v112, v112, v112 row_half_mirror row_mask:0xf bank_mask:0xf
	s_nop 1
	v_add_f32_dpp v112, v112, v112 row_mirror row_mask:0xf bank_mask:0xf
	v_fmamk_f32 v112, v112, 0x3a800000, v5
	v_rsq_f32_e32 v114, v112
	v_lshlrev_b32_e32 v116, 16, v92
	v_and_b32_e32 v117, 0xffff0000, v92
	v_lshlrev_b32_e32 v118, 16, v93
	v_and_b32_e32 v119, 0xffff0000, v93
	v_lshlrev_b32_e32 v120, 16, v94
	v_and_b32_e32 v121, 0xffff0000, v94
	v_lshlrev_b32_e32 v122, 16, v95
	v_and_b32_e32 v123, 0xffff0000, v95
	v_lshlrev_b32_e32 v124, 16, v96
	v_and_b32_e32 v125, 0xffff0000, v96
	v_lshlrev_b32_e32 v126, 16, v97
	v_and_b32_e32 v127, 0xffff0000, v97
	v_lshlrev_b32_e32 v128, 16, v98
	v_and_b32_e32 v129, 0xffff0000, v98
	v_lshlrev_b32_e32 v130, 16, v99
	v_and_b32_e32 v131, 0xffff0000, v99
	v_pk_mul_f32 v[116:117], v[114:115], v[116:117] op_sel_hi:[0,1]
	v_pk_mul_f32 v[118:119], v[114:115], v[118:119] op_sel_hi:[0,1]
	v_pk_mul_f32 v[120:121], v[114:115], v[120:121] op_sel_hi:[0,1]
	v_pk_mul_f32 v[122:123], v[114:115], v[122:123] op_sel_hi:[0,1]
	v_pk_mul_f32 v[124:125], v[114:115], v[124:125] op_sel_hi:[0,1]
	v_pk_mul_f32 v[126:127], v[114:115], v[126:127] op_sel_hi:[0,1]
	v_pk_mul_f32 v[128:129], v[114:115], v[128:129] op_sel_hi:[0,1]
	v_pk_mul_f32 v[130:131], v[114:115], v[130:131] op_sel_hi:[0,1]
	v_pk_mul_f32 v[132:133], v[8:9], v[116:117]
	v_pk_mul_f32 v[134:135], v[10:11], v[118:119]
	v_pk_mul_f32 v[136:137], v[12:13], v[120:121]
	v_pk_mul_f32 v[138:139], v[14:15], v[122:123]
	v_pk_mul_f32 v[140:141], v[16:17], v[124:125]
	v_pk_mul_f32 v[142:143], v[18:19], v[126:127]
	v_pk_mul_f32 v[144:145], v[20:21], v[128:129]
	v_pk_mul_f32 v[146:147], v[22:23], v[130:131]
	global_store_dwordx4 v2, v[132:135], s[34:35] offset:0
	global_store_dwordx4 v2, v[136:139], s[34:35] offset:1024
	global_store_dwordx4 v2, v[140:143], s[34:35] offset:2048
	global_store_dwordx4 v2, v[144:147], s[34:35] offset:3072
	s_waitcnt vmcnt(28)
	v_add_f32_dpp v112, v110, v110 quad_perm:[1,0,3,2] row_mask:0xf bank_mask:0xf
	s_mov_b64 s[36:37], s[24:25]
	s_add_u32 s24, s24, s22
	v_add_f32_dpp v112, v112, v112 quad_perm:[2,3,0,1] row_mask:0xf bank_mask:0xf
	s_addc_u32 s25, s25, 0
	s_nop 0
	v_add_f32_dpp v112, v112, v112 row_half_mirror row_mask:0xf bank_mask:0xf
	s_nop 1
	v_add_f32_dpp v112, v112, v112 row_mirror row_mask:0xf bank_mask:0xf
	v_fmamk_f32 v112, v112, 0x3a800000, v5
	v_rsq_f32_e32 v114, v112
	v_lshlrev_b32_e32 v116, 16, v102
	v_and_b32_e32 v117, 0xffff0000, v102
	v_lshlrev_b32_e32 v118, 16, v103
	v_and_b32_e32 v119, 0xffff0000, v103
	v_lshlrev_b32_e32 v120, 16, v104
	v_and_b32_e32 v121, 0xffff0000, v104
	v_lshlrev_b32_e32 v122, 16, v105
	v_and_b32_e32 v123, 0xffff0000, v105
	v_lshlrev_b32_e32 v124, 16, v106
	v_and_b32_e32 v125, 0xffff0000, v106
	v_lshlrev_b32_e32 v126, 16, v107
	v_and_b32_e32 v127, 0xffff0000, v107
	v_lshlrev_b32_e32 v128, 16, v108
	v_and_b32_e32 v129, 0xffff0000, v108
	v_lshlrev_b32_e32 v130, 16, v109
	v_and_b32_e32 v131, 0xffff0000, v109
	v_pk_mul_f32 v[116:117], v[114:115], v[116:117] op_sel_hi:[0,1]
	v_pk_mul_f32 v[118:119], v[114:115], v[118:119] op_sel_hi:[0,1]
	v_pk_mul_f32 v[120:121], v[114:115], v[120:121] op_sel_hi:[0,1]
	v_pk_mul_f32 v[122:123], v[114:115], v[122:123] op_sel_hi:[0,1]
	v_pk_mul_f32 v[124:125], v[114:115], v[124:125] op_sel_hi:[0,1]
	v_pk_mul_f32 v[126:127], v[114:115], v[126:127] op_sel_hi:[0,1]
	v_pk_mul_f32 v[128:129], v[114:115], v[128:129] op_sel_hi:[0,1]
	v_pk_mul_f32 v[130:131], v[114:115], v[130:131] op_sel_hi:[0,1]
	v_pk_mul_f32 v[132:133], v[8:9], v[116:117]
	v_pk_mul_f32 v[134:135], v[10:11], v[118:119]
	v_pk_mul_f32 v[136:137], v[12:13], v[120:121]
	v_pk_mul_f32 v[138:139], v[14:15], v[122:123]
	v_pk_mul_f32 v[140:141], v[16:17], v[124:125]
	v_pk_mul_f32 v[142:143], v[18:19], v[126:127]
	v_pk_mul_f32 v[144:145], v[20:21], v[128:129]
	v_pk_mul_f32 v[146:147], v[22:23], v[130:131]
	global_store_dwordx4 v2, v[132:135], s[36:37] offset:0
	global_store_dwordx4 v2, v[136:139], s[36:37] offset:1024
	global_store_dwordx4 v2, v[140:143], s[36:37] offset:2048
	global_store_dwordx4 v2, v[144:147], s[36:37] offset:3072
.Lfin_tail:
	s_cmp_lt_i32 s12, 0x10000
	s_cbranch_scc0 .LBB0_3641
	s_mov_b64 s[26:27], s[16:17]
	s_mov_b64 s[28:29], s[18:19]
	global_load_dword v40, v4, s[26:27]
	global_load_dwordx2 v[32:33], v3, s[28:29] offset:0
	global_load_dwordx2 v[34:35], v3, s[28:29] offset:512
	global_load_dwordx2 v[36:37], v3, s[28:29] offset:1024
	global_load_dwordx2 v[38:39], v3, s[28:29] offset:1536
	s_add_u32 s16, s16, s20
	s_addc_u32 s17, s17, 0
	s_add_u32 s18, s18, s21
	s_addc_u32 s19, s19, 0
	s_add_i32 s12, s12, s13
	s_waitcnt vmcnt(0)
	v_add_f32_dpp v112, v40, v40 quad_perm:[1,0,3,2] row_mask:0xf bank_mask:0xf
	s_mov_b64 s[34:35], s[24:25]
	s_add_u32 s24, s24, s22
	v_add_f32_dpp v112, v112, v112 quad_perm:[2,3,0,1] row_mask:0xf bank_mask:0xf
	s_addc_u32 s25, s25, 0
	s_nop 0
	v_add_f32_dpp v112, v112, v112 row_half_mirror row_mask:0xf bank_mask:0xf
	s_nop 1
	v_add_f32_dpp v112, v112, v112 row_mirror row_mask:0xf bank_mask:0xf
	v_fmamk_f32 v112, v112, 0x3a800000, v5
	v_rsq_f32_e32 v114, v112
	v_lshlrev_b32_e32 v116, 16, v32
	v_and_b32_e32 v117, 0xffff0000, v32
	v_lshlrev_b32_e32 v118, 16, v33
	v_and_b32_e32 v119, 0xffff0000, v33
	v_lshlrev_b32_e32 v120, 16, v34
	v_and_b32_e32 v121, 0xffff0000, v34
	v_lshlrev_b32_e32 v122, 16, v35
	v_and_b32_e32 v123, 0xffff0000, v35
	v_lshlrev_b32_e32 v124, 16, v36
	v_and_b32_e32 v125, 0xffff0000, v36
	v_lshlrev_b32_e32 v126, 16, v37
	v_and_b32_e32 v127, 0xffff0000, v37
	v_lshlrev_b32_e32 v128, 16, v38
	v_and_b32_e32 v129, 0xffff0000, v38
	v_lshlrev_b32_e32 v130, 16, v39
	v_and_b32_e32 v131, 0xffff0000, v39
	v_pk_mul_f32 v[116:117], v[114:115], v[116:117] op_sel_hi:[0,1]
	v_pk_mul_f32 v[118:119], v[114:115], v[118:119] op_sel_hi:[0,1]
	v_pk_mul_f32 v[120:121], v[114:115], v[120:121] op_sel_hi:[0,1]
	v_pk_mul_f32 v[122:123], v[114:115], v[122:123] op_sel_hi:[0,1]
	v_pk_mul_f32 v[124:125], v[114:115], v[124:125] op_sel_hi:[0,1]
	v_pk_mul_f32 v[126:127], v[114:115], v[126:127] op_sel_hi:[0,1]
	v_pk_mul_f32 v[128:129], v[114:115], v[128:129] op_sel_hi:[0,1]
	v_pk_mul_f32 v[130:131], v[114:115], v[130:131] op_sel_hi:[0,1]
	v_pk_mul_f32 v[132:133], v[8:9], v[116:117]
	v_pk_mul_f32 v[134:135], v[10:11], v[118:119]
	v_pk_mul_f32 v[136:137], v[12:13], v[120:121]
	v_pk_mul_f32 v[138:139], v[14:15], v[122:123]
	v_pk_mul_f32 v[140:141], v[16:17], v[124:125]
	v_pk_mul_f32 v[142:143], v[18:19], v[126:127]
	v_pk_mul_f32 v[144:145], v[20:21], v[128:129]
	v_pk_mul_f32 v[146:147], v[22:23], v[130:131]
	global_store_dwordx4 v2, v[132:135], s[34:35] offset:0
	global_store_dwordx4 v2, v[136:139], s[34:35] offset:1024
	global_store_dwordx4 v2, v[140:143], s[34:35] offset:2048
	global_store_dwordx4 v2, v[144:147], s[34:35] offset:3072
	s_branch .Lfin_tail
